# baseline (speedup 1.0000x reference)
.LBB3_32:
	s_or_b64 exec, exec, s[12:13]
	v_mov_b32_e32 v37, 0x22bc0
	s_waitcnt lgkmcnt(0)
	s_barrier
	ds_read_b128 v[38:41], v37
	v_mov_b32_e32 v37, 0x22c00
	ds_read_b128 v[42:45], v37
	s_movk_i32 s12, 0xfc
	s_waitcnt lgkmcnt(1)
	v_max_f32_e32 v37, v39, v39
	v_max_f32_e32 v38, v38, v38
	s_waitcnt lgkmcnt(0)
	v_max_f32_e32 v39, v42, v42
	v_mov_b32_e32 v42, 0x22bd0
	v_max_f32_e32 v37, v38, v37
	v_max_f32_e32 v38, v43, v43
	v_mov_b32_e32 v43, 0x22c10
	ds_read_b128 v[46:49], v42
	ds_read_b128 v[50:53], v43
	v_max_f32_e32 v38, v39, v38
	v_max3_f32 v38, v38, v44, v45
	v_max3_f32 v37, v37, v40, v41
	s_waitcnt lgkmcnt(1)
	v_max3_f32 v37, v37, v46, v47
	s_waitcnt lgkmcnt(0)
	v_max3_f32 v42, v38, v50, v51
	v_mov_b32_e32 v38, 0x22be0
	ds_read_b128 v[38:41], v38
	v_max3_f32 v54, v42, v52, v53
	v_mov_b32_e32 v42, 0x22c20
	v_max3_f32 v37, v37, v48, v49
	ds_read_b128 v[42:45], v42
	s_waitcnt lgkmcnt(1)
	v_max3_f32 v37, v37, v38, v39
	v_mov_b32_e32 v38, 0x22bf0
	v_mov_b32_e32 v39, 0x22c30
	ds_read_b128 v[46:49], v38
	ds_read_b128 v[50:53], v39
	s_waitcnt lgkmcnt(2)
	v_max3_f32 v38, v54, v42, v43
	v_max3_f32 v37, v37, v40, v41
	v_max3_f32 v38, v38, v44, v45
	s_waitcnt lgkmcnt(1)
	v_max3_f32 v37, v37, v46, v47
	s_waitcnt lgkmcnt(0)
	v_max3_f32 v39, v38, v50, v51
	v_max3_f32 v38, v37, v48, v49
	v_max3_f32 v39, v39, v52, v53
	v_and_b32_e32 v41, 0x7fffffff, v12
	v_and_b32_e32 v40, 0x7fffffff, v14
	v_pk_mul_f32 v[40:41], v[38:39], v[40:41]
	s_nop 0
	v_add_f32_e32 v37, v40, v41
	v_and_b32_e32 v41, 0x7fffffff, v13
	v_and_b32_e32 v40, 0x7fffffff, v15
	v_pk_mul_f32 v[40:41], v[38:39], v[40:41]
	v_add_f32_e64 v37, |v16|, v37
	v_add_f32_e32 v40, v40, v41
	v_add_f32_e64 v40, |v17|, v40
	v_max3_f32 v37, v37, 0, v40
	v_and_b32_e32 v41, 0x7fffffff, v6
	v_and_b32_e32 v40, 0x7fffffff, v8
	v_pk_mul_f32 v[40:41], v[38:39], v[40:41]
	s_nop 0
	v_add_f32_e32 v40, v40, v41
	v_add_f32_e64 v42, |v10|, v40
	v_and_b32_e32 v41, 0x7fffffff, v7
	v_and_b32_e32 v40, 0x7fffffff, v9
	v_pk_mul_f32 v[38:39], v[38:39], v[40:41]
	s_nop 0
	v_add_f32_e32 v38, v38, v39
	v_add_f32_e64 v38, |v11|, v38
	v_max3_f32 v37, v37, v42, v38
	v_max_f32_dpp v37, v37, v37 quad_perm:[1,0,3,2] row_mask:0xf bank_mask:0xf
	s_nop 1
	v_max_f32_dpp v37, v37, v37 quad_perm:[2,3,0,1] row_mask:0xf bank_mask:0xf
	s_nop 1
	v_max_f32_dpp v37, v37, v37 row_half_mirror row_mask:0xf bank_mask:0xf
	s_nop 1
	v_max_f32_dpp v37, v37, v37 row_mirror row_mask:0xf bank_mask:0xf
	s_nop 1
	v_max_f32_dpp v37, v37, v37 row_bcast:15 row_mask:0xa bank_mask:0xf
	s_nop 1
	v_max_f32_dpp v37, v37, v37 row_bcast:31 row_mask:0xc bank_mask:0xf
	s_nop 1
	v_readlane_b32 s14, v37, 63
	v_mov_b32_e32 v36, 0x800000
	s_nop 1
	v_mov_b32_e32 v2, s14
	v_bfe_u32 v3, v2, 23, 8
	v_lshlrev_b32_e32 v24, 23, v3
	v_sub_u32_e32 v24, 0x7e000000, v24
	v_cmp_gt_u32_e32 vcc, s12, v3
	v_cmp_neq_f32_e64 s[12:13], 0, v2
	s_nop 0
	v_cndmask_b32_e32 v3, v36, v24, vcc
	s_andn2_b64 vcc, exec, s[28:29]
	v_cndmask_b32_e64 v2, 1.0, v3, s[12:13]
	s_cbranch_vccnz .LBB3_39
	s_mov_b32 s12, 0x7ffffff8
	v_sub_u32_sdwa v36, v30, s24 dst_sel:DWORD dst_unused:UNUSED_PAD src0_sel:WORD_1 src1_sel:DWORD
	v_cndmask_b32_e64 v36, 0, v36, s[10:11]
	v_lshlrev_b32_e32 v36, 2, v36
	v_add_u32_e32 v48, 0x228a0, v36
	v_add_u32_e32 v49, 0x22580, v36
	ds_read_b32 v40, v48
	ds_read_b32 v44, v49
	v_sub_u32_sdwa v37, v27, s24 dst_sel:DWORD dst_unused:UNUSED_PAD src0_sel:WORD_1 src1_sel:DWORD
	v_cndmask_b32_e64 v37, 0, v37, s[8:9]
	v_lshlrev_b32_e32 v37, 2, v37
	v_add_u32_e32 v48, 0x228a0, v37
	v_add_u32_e32 v49, 0x22580, v37
	ds_read_b32 v41, v48
	ds_read_b32 v45, v49
	v_sub_u32_sdwa v38, v5, s24 dst_sel:DWORD dst_unused:UNUSED_PAD src0_sel:WORD_1 src1_sel:DWORD
	v_cndmask_b32_e64 v38, 0, v38, s[0:1]
	v_lshlrev_b32_e32 v38, 2, v38
	v_add_u32_e32 v48, 0x228a0, v38
	v_add_u32_e32 v49, 0x22580, v38
	ds_read_b32 v42, v48
	ds_read_b32 v46, v49
	v_sub_u32_sdwa v39, v4, s24 dst_sel:DWORD dst_unused:UNUSED_PAD src0_sel:WORD_1 src1_sel:DWORD
	v_cndmask_b32_e64 v39, 0, v39, s[6:7]
	v_lshlrev_b32_e32 v39, 2, v39
	v_add_u32_e32 v48, 0x228a0, v39
	v_add_u32_e32 v49, 0x22580, v39
	ds_read_b32 v43, v48
	ds_read_b32 v47, v49
	s_waitcnt lgkmcnt(6)
	v_sub_u32_e32 v40, v20, v40
	v_lshlrev_b32_e32 v44, 3, v44
	v_add_u32_e32 v40, v0, v40
	v_lshl_add_u32 v44, v40, 1, v44
	v_and_b32_e32 v48, 1, v40
	v_lshlrev_b32_e32 v40, 2, v40
	v_and_or_b32 v44, v44, s12, v48
	v_and_b32_e32 v40, 8, v40
	v_lshl_or_b32 v40, v44, 1, v40
	v_add_u32_e32 v40, 0x1ce00, v40
	v_fma_mixlo_f16 v35, v35, v2, 0
	v_fma_mixlo_f16 v34, v34, v2, 0
	s_and_saveexec_b64 s[14:15], s[10:11]
	ds_write_b16 v40, v35
	ds_write_b16 v40, v34 offset:4
	s_or_b64 exec, exec, s[14:15]
	s_waitcnt lgkmcnt(6)
	v_sub_u32_e32 v41, v20, v41
	v_lshlrev_b32_e32 v45, 3, v45
	v_add_u32_e32 v41, v23, v41
	v_lshl_add_u32 v45, v41, 1, v45
	v_and_b32_e32 v48, 1, v41
	v_lshlrev_b32_e32 v41, 2, v41
	v_and_or_b32 v45, v45, s12, v48
	v_and_b32_e32 v41, 8, v41
	v_lshl_or_b32 v41, v45, 1, v41
	v_add_u32_e32 v41, 0x1ce00, v41
	v_fma_mixlo_f16 v32, v32, v2, 0
	v_fma_mixlo_f16 v31, v31, v2, 0
	s_and_saveexec_b64 s[14:15], s[8:9]
	ds_write_b16 v41, v32
	ds_write_b16 v41, v31 offset:4
	s_or_b64 exec, exec, s[14:15]
	s_waitcnt lgkmcnt(6)
	v_sub_u32_e32 v42, v20, v42
	v_lshlrev_b32_e32 v46, 3, v46
	v_add_u32_e32 v42, v22, v42
	v_lshl_add_u32 v46, v42, 1, v46
	v_and_b32_e32 v48, 1, v42
	v_lshlrev_b32_e32 v42, 2, v42
	v_and_or_b32 v46, v46, s12, v48
	v_and_b32_e32 v42, 8, v42
	v_lshl_or_b32 v42, v46, 1, v42
	v_add_u32_e32 v42, 0x1ce00, v42
	v_fma_mixlo_f16 v29, v29, v2, 0
	v_fma_mixlo_f16 v28, v28, v2, 0
	s_and_saveexec_b64 s[14:15], s[0:1]
	ds_write_b16 v42, v29
	ds_write_b16 v42, v28 offset:4
	s_or_b64 exec, exec, s[14:15]
	s_waitcnt lgkmcnt(6)
	v_sub_u32_e32 v43, v20, v43
	v_lshlrev_b32_e32 v47, 3, v47
	v_add_u32_e32 v43, v21, v43
	v_lshl_add_u32 v47, v43, 1, v47
	v_and_b32_e32 v48, 1, v43
	v_lshlrev_b32_e32 v43, 2, v43
	v_and_or_b32 v47, v47, s12, v48
	v_and_b32_e32 v43, 8, v43
	v_lshl_or_b32 v43, v47, 1, v43
	v_add_u32_e32 v43, 0x1ce00, v43
	v_fma_mixlo_f16 v26, v26, v2, 0
	v_fma_mixlo_f16 v25, v25, v2, 0
	s_and_saveexec_b64 s[14:15], s[6:7]
	ds_write_b16 v43, v26
	ds_write_b16 v43, v25 offset:4
	s_or_b64 exec, exec, s[14:15]
.LBB3_35:
.LBB3_36:
.LBB3_37:
.LBB3_38:
.LBB3_39:
	v_cvt_f16_f32_e32 v3, v14
	v_cvt_f16_f32_e32 v4, v12
	v_mul_f32_e32 v21, v16, v2
	v_fma_mixlo_f16 v5, v16, v2, 0
	v_mul_u32_u24_e32 v16, 0x10001, v3
	v_mul_u32_u24_e32 v22, 0x10001, v4
	v_cvt_f16_f32_e32 v3, v15
	v_cvt_f16_f32_e32 v4, v13
	s_mov_b32 s0, 0x10001
	v_mul_u32_u24_sdwa v23, v5, s0 dst_sel:DWORD dst_unused:UNUSED_PAD src0_sel:WORD_0 src1_sel:DWORD
	v_mul_f32_e32 v24, v17, v2
	v_fma_mixlo_f16 v5, v17, v2, 0
	v_mul_u32_u24_e32 v17, 0x10001, v3
	v_mul_u32_u24_e32 v25, 0x10001, v4
	v_cvt_f16_f32_e32 v3, v8
	v_cvt_f16_f32_e32 v4, v6
	v_mul_u32_u24_sdwa v26, v5, s0 dst_sel:DWORD dst_unused:UNUSED_PAD src0_sel:WORD_0 src1_sel:DWORD
	v_mul_f32_e32 v27, v10, v2
	v_fma_mixlo_f16 v5, v10, v2, 0
	v_mul_u32_u24_e32 v10, 0x10001, v3
	v_mul_u32_u24_e32 v28, 0x10001, v4
	v_cvt_f16_f32_e32 v3, v9
	v_cvt_f16_f32_e32 v4, v7
	v_sub_u32_e32 v20, 0x7f000000, v2
	v_mul_f32_e32 v14, v14, v2
	v_mul_f32_e32 v12, v12, v2
	v_mul_f32_e32 v15, v15, v2
	v_mul_f32_e32 v13, v13, v2
	v_mul_u32_u24_sdwa v29, v5, s0 dst_sel:DWORD dst_unused:UNUSED_PAD src0_sel:WORD_0 src1_sel:DWORD
	v_mul_f32_e32 v8, v8, v2
	v_mul_f32_e32 v6, v6, v2
	v_mul_f32_e32 v30, v11, v2
	v_fma_mixlo_f16 v5, v11, v2, 0
	v_mul_f32_e32 v9, v9, v2
	v_mul_f32_e32 v7, v7, v2
	v_cndmask_b32_e64 v2, 0, 1, s[26:27]
	v_mul_u32_u24_e32 v11, 0x10001, v3
	v_mul_u32_u24_e32 v31, 0x10001, v4
	v_mul_u32_u24_sdwa v32, v5, s0 dst_sel:DWORD dst_unused:UNUSED_PAD src0_sel:WORD_0 src1_sel:DWORD
	v_lshlrev_b32_e32 v33, 1, v33
	v_mov_b32_e32 v34, 0x22c50
	v_cmp_ne_u32_e64 s[6:7], 1, v2
	s_movk_i32 s12, 0x3c00
	v_mov_b32_e32 v35, 0x3c00
	s_sub_i32 s34, 0xe0, s3
	s_mul_i32 s35, s34, 33
	s_mul_i32 s36, s3, 0x210
	v_mov_b32_e32 v104, 0
	v_mov_b32_e32 v105, 0
	v_mov_b32_e32 v106, 0
	v_mov_b32_e32 v107, 0
	v_mov_b32_e32 v108, v0
	v_lshlrev_b32_e32 v109, 4, v0
	v_add_u32_e32 v109, s36, v109
	s_mov_b64 s[36:37], exec
